# ml_scan: loads of both 16-chunk halves issued up front, 32-step scan with counted waits
# baseline (speedup 1.0000x reference)
.LBB0_485:
	v_mov_b32_e32 v6, v22
	v_ashrrev_i32_e32 v7, 31, v6
	v_mad_i64_i32 v[8:9], s[14:15], v6, s8, v[14:15]
	v_lshl_add_u64 v[6:7], v[6:7], 2, s[0:1]
	global_load_dwordx2 v[36:37], v[8:9], off
	global_load_dword v10, v[6:7], off
	v_lshl_add_u64 v[20:21], s[54:55], 0, v[16:17]
	v_lshl_add_u64 v[6:7], s[54:55], 0, v[18:19]
	s_mov_b64 s[14:15], 0x1400000
	v_lshl_add_u64 v[6:7], v[6:7], 0, s[14:15]
	global_load_dwordx4 v[68:71], v[6:7], off
	global_load_dwordx4 v[72:75], v[6:7], off offset:16
	global_load_dwordx4 v[76:79], v[6:7], off offset:32
	global_load_dwordx3 v[80:82], v[6:7], off offset:48
	s_mov_b64 s[14:15], 0xae80000
	v_lshl_add_u64 v[38:39], v[20:21], 0, s[14:15]
	global_load_dwordx2 v[38:39], v[38:39], off
	s_mov_b64 s[14:15], 0xae91000
	v_lshl_add_u64 v[40:41], v[20:21], 0, s[14:15]
	global_load_dwordx2 v[40:41], v[40:41], off
	s_mov_b64 s[14:15], 0xaea2000
	v_lshl_add_u64 v[42:43], v[20:21], 0, s[14:15]
	global_load_dwordx2 v[42:43], v[42:43], off
	s_mov_b64 s[14:15], 0xaeb3000
	v_lshl_add_u64 v[44:45], v[20:21], 0, s[14:15]
	global_load_dwordx2 v[44:45], v[44:45], off
	s_mov_b64 s[14:15], 0xaec4000
	v_lshl_add_u64 v[46:47], v[20:21], 0, s[14:15]
	global_load_dwordx2 v[46:47], v[46:47], off
	s_mov_b64 s[14:15], 0xaed5000
	v_lshl_add_u64 v[48:49], v[20:21], 0, s[14:15]
	global_load_dwordx2 v[48:49], v[48:49], off
	s_mov_b64 s[14:15], 0xaee6000
	v_lshl_add_u64 v[50:51], v[20:21], 0, s[14:15]
	global_load_dwordx2 v[50:51], v[50:51], off
	s_mov_b64 s[14:15], 0xaef7000
	v_lshl_add_u64 v[52:53], v[20:21], 0, s[14:15]
	global_load_dwordx2 v[52:53], v[52:53], off
	s_mov_b64 s[14:15], 0xaf08000
	v_lshl_add_u64 v[54:55], v[20:21], 0, s[14:15]
	global_load_dwordx2 v[54:55], v[54:55], off
	s_mov_b64 s[14:15], 0xaf19000
	v_lshl_add_u64 v[56:57], v[20:21], 0, s[14:15]
	global_load_dwordx2 v[56:57], v[56:57], off
	s_mov_b64 s[14:15], 0xaf2a000
	v_lshl_add_u64 v[58:59], v[20:21], 0, s[14:15]
	global_load_dwordx2 v[58:59], v[58:59], off
	s_mov_b64 s[14:15], 0xaf3b000
	v_lshl_add_u64 v[60:61], v[20:21], 0, s[14:15]
	global_load_dwordx2 v[60:61], v[60:61], off
	s_mov_b64 s[14:15], 0xaf4c000
	v_lshl_add_u64 v[62:63], v[20:21], 0, s[14:15]
	global_load_dwordx2 v[62:63], v[62:63], off
	s_mov_b64 s[14:15], 0xaf5d000
	v_lshl_add_u64 v[64:65], v[20:21], 0, s[14:15]
	global_load_dwordx2 v[64:65], v[64:65], off
	s_mov_b64 s[14:15], 0xaf6e000
	v_lshl_add_u64 v[66:67], v[20:21], 0, s[14:15]
	global_load_dwordx2 v[66:67], v[66:67], off
	v_add_u32_e32 v6, 16, v23
	v_ashrrev_i32_e32 v7, 31, v6
	v_mad_i64_i32 v[8:9], s[14:15], v6, s8, v[14:15]
	v_lshl_add_u64 v[6:7], v[6:7], 2, s[0:1]
	global_load_dwordx2 v[84:85], v[8:9], off
	global_load_dword v107, v[6:7], off
	s_mov_b64 s[14:15], 0x110000
	v_lshl_add_u64 v[24:25], v[20:21], 0, s[14:15]
	v_lshl_add_u64 v[6:7], s[54:55], 0, v[18:19]
	s_mov_b64 s[14:15], 0x1400040
	v_lshl_add_u64 v[6:7], v[6:7], 0, s[14:15]
	global_load_dwordx4 v[118:121], v[6:7], off
	global_load_dwordx4 v[122:125], v[6:7], off offset:16
	global_load_dwordx4 v[126:129], v[6:7], off offset:32
	global_load_dwordx3 v[26:28], v[6:7], off offset:48
	s_mov_b64 s[14:15], 0xae80000
	v_lshl_add_u64 v[86:87], v[24:25], 0, s[14:15]
	global_load_dwordx2 v[86:87], v[86:87], off
	s_mov_b64 s[14:15], 0xae91000
	v_lshl_add_u64 v[88:89], v[24:25], 0, s[14:15]
	global_load_dwordx2 v[88:89], v[88:89], off
	s_mov_b64 s[14:15], 0xaea2000
	v_lshl_add_u64 v[90:91], v[24:25], 0, s[14:15]
	global_load_dwordx2 v[90:91], v[90:91], off
	s_mov_b64 s[14:15], 0xaeb3000
	v_lshl_add_u64 v[92:93], v[24:25], 0, s[14:15]
	global_load_dwordx2 v[92:93], v[92:93], off
	s_mov_b64 s[14:15], 0xaec4000
	v_lshl_add_u64 v[94:95], v[24:25], 0, s[14:15]
	global_load_dwordx2 v[94:95], v[94:95], off
	s_mov_b64 s[14:15], 0xaed5000
	v_lshl_add_u64 v[96:97], v[24:25], 0, s[14:15]
	global_load_dwordx2 v[96:97], v[96:97], off
	s_mov_b64 s[14:15], 0xaee6000
	v_lshl_add_u64 v[98:99], v[24:25], 0, s[14:15]
	global_load_dwordx2 v[98:99], v[98:99], off
	s_mov_b64 s[14:15], 0xaef7000
	v_lshl_add_u64 v[100:101], v[24:25], 0, s[14:15]
	global_load_dwordx2 v[100:101], v[100:101], off
	s_mov_b64 s[14:15], 0xaf08000
	v_lshl_add_u64 v[102:103], v[24:25], 0, s[14:15]
	global_load_dwordx2 v[102:103], v[102:103], off
	s_mov_b64 s[14:15], 0xaf19000
	v_lshl_add_u64 v[104:105], v[24:25], 0, s[14:15]
	global_load_dwordx2 v[104:105], v[104:105], off
	s_mov_b64 s[14:15], 0xaf2a000
	v_lshl_add_u64 v[108:109], v[24:25], 0, s[14:15]
	global_load_dwordx2 v[108:109], v[108:109], off
	s_mov_b64 s[14:15], 0xaf3b000
	v_lshl_add_u64 v[110:111], v[24:25], 0, s[14:15]
	global_load_dwordx2 v[110:111], v[110:111], off
	s_mov_b64 s[14:15], 0xaf4c000
	v_lshl_add_u64 v[112:113], v[24:25], 0, s[14:15]
	global_load_dwordx2 v[112:113], v[112:113], off
	s_mov_b64 s[14:15], 0xaf5d000
	v_lshl_add_u64 v[114:115], v[24:25], 0, s[14:15]
	global_load_dwordx2 v[114:115], v[114:115], off
	s_mov_b64 s[14:15], 0xaf6e000
	v_lshl_add_u64 v[116:117], v[24:25], 0, s[14:15]
	global_load_dwordx2 v[116:117], v[116:117], off
	s_waitcnt vmcnt(40)
	v_mul_f32_e32 v10, 0x3fb8aa3b, v10
	v_exp_f32_e32 v10, v10
	v_lshlrev_b32_e32 v8, 16, v36
	v_and_b32_e32 v9, 0xffff0000, v36
	v_lshlrev_b32_e32 v32, 16, v37
	v_and_b32_e32 v33, 0xffff0000, v37
	v_pk_fma_f32 v[2:3], v[2:3], v[10:11], v[8:9] op_sel_hi:[1,0,1]
	v_pk_fma_f32 v[4:5], v[4:5], v[10:11], v[32:33] op_sel_hi:[1,0,1]
	s_mov_b64 s[14:15], 0x9d00000
	v_lshl_add_u64 v[8:9], v[20:21], 0, s[14:15]
	v_cvt_pk_bf16_f32 v6, v2, v3
	v_cvt_pk_bf16_f32 v7, v4, v5
	global_store_dwordx2 v[8:9], v[6:7], off sc1
	s_waitcnt vmcnt(36)
	v_mul_f32_e32 v10, 0x3fb8aa3b, v68
	v_exp_f32_e32 v10, v10
	v_lshlrev_b32_e32 v8, 16, v38
	v_and_b32_e32 v9, 0xffff0000, v38
	v_lshlrev_b32_e32 v32, 16, v39
	v_and_b32_e32 v33, 0xffff0000, v39
	v_pk_fma_f32 v[2:3], v[2:3], v[10:11], v[8:9] op_sel_hi:[1,0,1]
	v_pk_fma_f32 v[4:5], v[4:5], v[10:11], v[32:33] op_sel_hi:[1,0,1]
	s_mov_b64 s[14:15], 0x9d11000
	v_lshl_add_u64 v[8:9], v[20:21], 0, s[14:15]
	v_cvt_pk_bf16_f32 v6, v2, v3
	v_cvt_pk_bf16_f32 v7, v4, v5
	global_store_dwordx2 v[8:9], v[6:7], off sc1
	s_waitcnt vmcnt(36)
	v_mul_f32_e32 v10, 0x3fb8aa3b, v69
	v_exp_f32_e32 v10, v10
	v_lshlrev_b32_e32 v8, 16, v40
	v_and_b32_e32 v9, 0xffff0000, v40
	v_lshlrev_b32_e32 v32, 16, v41
	v_and_b32_e32 v33, 0xffff0000, v41
	v_pk_fma_f32 v[2:3], v[2:3], v[10:11], v[8:9] op_sel_hi:[1,0,1]
	v_pk_fma_f32 v[4:5], v[4:5], v[10:11], v[32:33] op_sel_hi:[1,0,1]
	s_mov_b64 s[14:15], 0x9d22000
	v_lshl_add_u64 v[8:9], v[20:21], 0, s[14:15]
	v_cvt_pk_bf16_f32 v6, v2, v3
	v_cvt_pk_bf16_f32 v7, v4, v5
	global_store_dwordx2 v[8:9], v[6:7], off sc1
	s_waitcnt vmcnt(36)
	v_mul_f32_e32 v10, 0x3fb8aa3b, v70
	v_exp_f32_e32 v10, v10
	v_lshlrev_b32_e32 v8, 16, v42
	v_and_b32_e32 v9, 0xffff0000, v42
	v_lshlrev_b32_e32 v32, 16, v43
	v_and_b32_e32 v33, 0xffff0000, v43
	v_pk_fma_f32 v[2:3], v[2:3], v[10:11], v[8:9] op_sel_hi:[1,0,1]
	v_pk_fma_f32 v[4:5], v[4:5], v[10:11], v[32:33] op_sel_hi:[1,0,1]
	s_mov_b64 s[14:15], 0x9d33000
	v_lshl_add_u64 v[8:9], v[20:21], 0, s[14:15]
	v_cvt_pk_bf16_f32 v6, v2, v3
	v_cvt_pk_bf16_f32 v7, v4, v5
	global_store_dwordx2 v[8:9], v[6:7], off sc1
	s_waitcnt vmcnt(36)
	v_mul_f32_e32 v10, 0x3fb8aa3b, v71
	v_exp_f32_e32 v10, v10
	v_lshlrev_b32_e32 v8, 16, v44
	v_and_b32_e32 v9, 0xffff0000, v44
	v_lshlrev_b32_e32 v32, 16, v45
	v_and_b32_e32 v33, 0xffff0000, v45
	v_pk_fma_f32 v[2:3], v[2:3], v[10:11], v[8:9] op_sel_hi:[1,0,1]
	v_pk_fma_f32 v[4:5], v[4:5], v[10:11], v[32:33] op_sel_hi:[1,0,1]
	s_mov_b64 s[14:15], 0x9d44000
	v_lshl_add_u64 v[8:9], v[20:21], 0, s[14:15]
	v_cvt_pk_bf16_f32 v6, v2, v3
	v_cvt_pk_bf16_f32 v7, v4, v5
	global_store_dwordx2 v[8:9], v[6:7], off sc1
	s_waitcnt vmcnt(36)
	v_mul_f32_e32 v10, 0x3fb8aa3b, v72
	v_exp_f32_e32 v10, v10
	v_lshlrev_b32_e32 v8, 16, v46
	v_and_b32_e32 v9, 0xffff0000, v46
	v_lshlrev_b32_e32 v32, 16, v47
	v_and_b32_e32 v33, 0xffff0000, v47
	v_pk_fma_f32 v[2:3], v[2:3], v[10:11], v[8:9] op_sel_hi:[1,0,1]
	v_pk_fma_f32 v[4:5], v[4:5], v[10:11], v[32:33] op_sel_hi:[1,0,1]
	s_mov_b64 s[14:15], 0x9d55000
	v_lshl_add_u64 v[8:9], v[20:21], 0, s[14:15]
	v_cvt_pk_bf16_f32 v6, v2, v3
	v_cvt_pk_bf16_f32 v7, v4, v5
	global_store_dwordx2 v[8:9], v[6:7], off sc1
	s_waitcnt vmcnt(36)
	v_mul_f32_e32 v10, 0x3fb8aa3b, v73
	v_exp_f32_e32 v10, v10
	v_lshlrev_b32_e32 v8, 16, v48
	v_and_b32_e32 v9, 0xffff0000, v48
	v_lshlrev_b32_e32 v32, 16, v49
	v_and_b32_e32 v33, 0xffff0000, v49
	v_pk_fma_f32 v[2:3], v[2:3], v[10:11], v[8:9] op_sel_hi:[1,0,1]
	v_pk_fma_f32 v[4:5], v[4:5], v[10:11], v[32:33] op_sel_hi:[1,0,1]
	s_mov_b64 s[14:15], 0x9d66000
	v_lshl_add_u64 v[8:9], v[20:21], 0, s[14:15]
	v_cvt_pk_bf16_f32 v6, v2, v3
	v_cvt_pk_bf16_f32 v7, v4, v5
	global_store_dwordx2 v[8:9], v[6:7], off sc1
	s_waitcnt vmcnt(36)
	v_mul_f32_e32 v10, 0x3fb8aa3b, v74
	v_exp_f32_e32 v10, v10
	v_lshlrev_b32_e32 v8, 16, v50
	v_and_b32_e32 v9, 0xffff0000, v50
	v_lshlrev_b32_e32 v32, 16, v51
	v_and_b32_e32 v33, 0xffff0000, v51
	v_pk_fma_f32 v[2:3], v[2:3], v[10:11], v[8:9] op_sel_hi:[1,0,1]
	v_pk_fma_f32 v[4:5], v[4:5], v[10:11], v[32:33] op_sel_hi:[1,0,1]
	s_mov_b64 s[14:15], 0x9d77000
	v_lshl_add_u64 v[8:9], v[20:21], 0, s[14:15]
	v_cvt_pk_bf16_f32 v6, v2, v3
	v_cvt_pk_bf16_f32 v7, v4, v5
	global_store_dwordx2 v[8:9], v[6:7], off sc1
	s_waitcnt vmcnt(36)
	v_mul_f32_e32 v10, 0x3fb8aa3b, v75
	v_exp_f32_e32 v10, v10
	v_lshlrev_b32_e32 v8, 16, v52
	v_and_b32_e32 v9, 0xffff0000, v52
	v_lshlrev_b32_e32 v32, 16, v53
	v_and_b32_e32 v33, 0xffff0000, v53
	v_pk_fma_f32 v[2:3], v[2:3], v[10:11], v[8:9] op_sel_hi:[1,0,1]
	v_pk_fma_f32 v[4:5], v[4:5], v[10:11], v[32:33] op_sel_hi:[1,0,1]
	s_mov_b64 s[14:15], 0x9d88000
	v_lshl_add_u64 v[8:9], v[20:21], 0, s[14:15]
	v_cvt_pk_bf16_f32 v6, v2, v3
	v_cvt_pk_bf16_f32 v7, v4, v5
	global_store_dwordx2 v[8:9], v[6:7], off sc1
	s_waitcnt vmcnt(36)
	v_mul_f32_e32 v10, 0x3fb8aa3b, v76
	v_exp_f32_e32 v10, v10
	v_lshlrev_b32_e32 v8, 16, v54
	v_and_b32_e32 v9, 0xffff0000, v54
	v_lshlrev_b32_e32 v32, 16, v55
	v_and_b32_e32 v33, 0xffff0000, v55
	v_pk_fma_f32 v[2:3], v[2:3], v[10:11], v[8:9] op_sel_hi:[1,0,1]
	v_pk_fma_f32 v[4:5], v[4:5], v[10:11], v[32:33] op_sel_hi:[1,0,1]
	s_mov_b64 s[14:15], 0x9d99000
	v_lshl_add_u64 v[8:9], v[20:21], 0, s[14:15]
	v_cvt_pk_bf16_f32 v6, v2, v3
	v_cvt_pk_bf16_f32 v7, v4, v5
	global_store_dwordx2 v[8:9], v[6:7], off sc1
	s_waitcnt vmcnt(36)
	v_mul_f32_e32 v10, 0x3fb8aa3b, v77
	v_exp_f32_e32 v10, v10
	v_lshlrev_b32_e32 v8, 16, v56
	v_and_b32_e32 v9, 0xffff0000, v56
	v_lshlrev_b32_e32 v32, 16, v57
	v_and_b32_e32 v33, 0xffff0000, v57
	v_pk_fma_f32 v[2:3], v[2:3], v[10:11], v[8:9] op_sel_hi:[1,0,1]
	v_pk_fma_f32 v[4:5], v[4:5], v[10:11], v[32:33] op_sel_hi:[1,0,1]
	s_mov_b64 s[14:15], 0x9daa000
	v_lshl_add_u64 v[8:9], v[20:21], 0, s[14:15]
	v_cvt_pk_bf16_f32 v6, v2, v3
	v_cvt_pk_bf16_f32 v7, v4, v5
	global_store_dwordx2 v[8:9], v[6:7], off sc1
	s_waitcnt vmcnt(36)
	v_mul_f32_e32 v10, 0x3fb8aa3b, v78
	v_exp_f32_e32 v10, v10
	v_lshlrev_b32_e32 v8, 16, v58
	v_and_b32_e32 v9, 0xffff0000, v58
	v_lshlrev_b32_e32 v32, 16, v59
	v_and_b32_e32 v33, 0xffff0000, v59
	v_pk_fma_f32 v[2:3], v[2:3], v[10:11], v[8:9] op_sel_hi:[1,0,1]
	v_pk_fma_f32 v[4:5], v[4:5], v[10:11], v[32:33] op_sel_hi:[1,0,1]
	s_mov_b64 s[14:15], 0x9dbb000
	v_lshl_add_u64 v[8:9], v[20:21], 0, s[14:15]
	v_cvt_pk_bf16_f32 v6, v2, v3
	v_cvt_pk_bf16_f32 v7, v4, v5
	global_store_dwordx2 v[8:9], v[6:7], off sc1
	s_waitcnt vmcnt(36)
	v_mul_f32_e32 v10, 0x3fb8aa3b, v79
	v_exp_f32_e32 v10, v10
	v_lshlrev_b32_e32 v8, 16, v60
	v_and_b32_e32 v9, 0xffff0000, v60
	v_lshlrev_b32_e32 v32, 16, v61
	v_and_b32_e32 v33, 0xffff0000, v61
	v_pk_fma_f32 v[2:3], v[2:3], v[10:11], v[8:9] op_sel_hi:[1,0,1]
	v_pk_fma_f32 v[4:5], v[4:5], v[10:11], v[32:33] op_sel_hi:[1,0,1]
	s_mov_b64 s[14:15], 0x9dcc000
	v_lshl_add_u64 v[8:9], v[20:21], 0, s[14:15]
	v_cvt_pk_bf16_f32 v6, v2, v3
	v_cvt_pk_bf16_f32 v7, v4, v5
	global_store_dwordx2 v[8:9], v[6:7], off sc1
	s_waitcnt vmcnt(36)
	v_mul_f32_e32 v10, 0x3fb8aa3b, v80
	v_exp_f32_e32 v10, v10
	v_lshlrev_b32_e32 v8, 16, v62
	v_and_b32_e32 v9, 0xffff0000, v62
	v_lshlrev_b32_e32 v32, 16, v63
	v_and_b32_e32 v33, 0xffff0000, v63
	v_pk_fma_f32 v[2:3], v[2:3], v[10:11], v[8:9] op_sel_hi:[1,0,1]
	v_pk_fma_f32 v[4:5], v[4:5], v[10:11], v[32:33] op_sel_hi:[1,0,1]
	s_mov_b64 s[14:15], 0x9ddd000
	v_lshl_add_u64 v[8:9], v[20:21], 0, s[14:15]
	v_cvt_pk_bf16_f32 v6, v2, v3
	v_cvt_pk_bf16_f32 v7, v4, v5
	global_store_dwordx2 v[8:9], v[6:7], off sc1
	s_waitcnt vmcnt(36)
	v_mul_f32_e32 v10, 0x3fb8aa3b, v81
	v_exp_f32_e32 v10, v10
	v_lshlrev_b32_e32 v8, 16, v64
	v_and_b32_e32 v9, 0xffff0000, v64
	v_lshlrev_b32_e32 v32, 16, v65
	v_and_b32_e32 v33, 0xffff0000, v65
	v_pk_fma_f32 v[2:3], v[2:3], v[10:11], v[8:9] op_sel_hi:[1,0,1]
	v_pk_fma_f32 v[4:5], v[4:5], v[10:11], v[32:33] op_sel_hi:[1,0,1]
	s_mov_b64 s[14:15], 0x9dee000
	v_lshl_add_u64 v[8:9], v[20:21], 0, s[14:15]
	v_cvt_pk_bf16_f32 v6, v2, v3
	v_cvt_pk_bf16_f32 v7, v4, v5
	global_store_dwordx2 v[8:9], v[6:7], off sc1
	s_waitcnt vmcnt(36)
	v_mul_f32_e32 v10, 0x3fb8aa3b, v82
	v_exp_f32_e32 v10, v10
	v_lshlrev_b32_e32 v8, 16, v66
	v_and_b32_e32 v9, 0xffff0000, v66
	v_lshlrev_b32_e32 v32, 16, v67
	v_and_b32_e32 v33, 0xffff0000, v67
	v_pk_fma_f32 v[2:3], v[2:3], v[10:11], v[8:9] op_sel_hi:[1,0,1]
	v_pk_fma_f32 v[4:5], v[4:5], v[10:11], v[32:33] op_sel_hi:[1,0,1]
	s_mov_b64 s[14:15], 0x9dff000
	v_lshl_add_u64 v[8:9], v[20:21], 0, s[14:15]
	v_cvt_pk_bf16_f32 v6, v2, v3
	v_cvt_pk_bf16_f32 v7, v4, v5
	global_store_dwordx2 v[8:9], v[6:7], off sc1
	s_waitcnt vmcnt(35)
	v_mul_f32_e32 v10, 0x3fb8aa3b, v107
	v_exp_f32_e32 v10, v10
	v_lshlrev_b32_e32 v8, 16, v84
	v_and_b32_e32 v9, 0xffff0000, v84
	v_lshlrev_b32_e32 v32, 16, v85
	v_and_b32_e32 v33, 0xffff0000, v85
	v_pk_fma_f32 v[2:3], v[2:3], v[10:11], v[8:9] op_sel_hi:[1,0,1]
	v_pk_fma_f32 v[4:5], v[4:5], v[10:11], v[32:33] op_sel_hi:[1,0,1]
	s_mov_b64 s[14:15], 0x9d00000
	v_lshl_add_u64 v[8:9], v[24:25], 0, s[14:15]
	v_cvt_pk_bf16_f32 v6, v2, v3
	v_cvt_pk_bf16_f32 v7, v4, v5
	global_store_dwordx2 v[8:9], v[6:7], off sc1
	s_waitcnt vmcnt(31)
	v_mul_f32_e32 v10, 0x3fb8aa3b, v118
	v_exp_f32_e32 v10, v10
	v_lshlrev_b32_e32 v8, 16, v86
	v_and_b32_e32 v9, 0xffff0000, v86
	v_lshlrev_b32_e32 v32, 16, v87
	v_and_b32_e32 v33, 0xffff0000, v87
	v_pk_fma_f32 v[2:3], v[2:3], v[10:11], v[8:9] op_sel_hi:[1,0,1]
	v_pk_fma_f32 v[4:5], v[4:5], v[10:11], v[32:33] op_sel_hi:[1,0,1]
	s_mov_b64 s[14:15], 0x9d11000
	v_lshl_add_u64 v[8:9], v[24:25], 0, s[14:15]
	v_cvt_pk_bf16_f32 v6, v2, v3
	v_cvt_pk_bf16_f32 v7, v4, v5
	global_store_dwordx2 v[8:9], v[6:7], off sc1
	s_waitcnt vmcnt(31)
	v_mul_f32_e32 v10, 0x3fb8aa3b, v119
	v_exp_f32_e32 v10, v10
	v_lshlrev_b32_e32 v8, 16, v88
	v_and_b32_e32 v9, 0xffff0000, v88
	v_lshlrev_b32_e32 v32, 16, v89
	v_and_b32_e32 v33, 0xffff0000, v89
	v_pk_fma_f32 v[2:3], v[2:3], v[10:11], v[8:9] op_sel_hi:[1,0,1]
	v_pk_fma_f32 v[4:5], v[4:5], v[10:11], v[32:33] op_sel_hi:[1,0,1]
	s_mov_b64 s[14:15], 0x9d22000
	v_lshl_add_u64 v[8:9], v[24:25], 0, s[14:15]
	v_cvt_pk_bf16_f32 v6, v2, v3
	v_cvt_pk_bf16_f32 v7, v4, v5
	global_store_dwordx2 v[8:9], v[6:7], off sc1
	s_waitcnt vmcnt(31)
	v_mul_f32_e32 v10, 0x3fb8aa3b, v120
	v_exp_f32_e32 v10, v10
	v_lshlrev_b32_e32 v8, 16, v90
	v_and_b32_e32 v9, 0xffff0000, v90
	v_lshlrev_b32_e32 v32, 16, v91
	v_and_b32_e32 v33, 0xffff0000, v91
	v_pk_fma_f32 v[2:3], v[2:3], v[10:11], v[8:9] op_sel_hi:[1,0,1]
	v_pk_fma_f32 v[4:5], v[4:5], v[10:11], v[32:33] op_sel_hi:[1,0,1]
	s_mov_b64 s[14:15], 0x9d33000
	v_lshl_add_u64 v[8:9], v[24:25], 0, s[14:15]
	v_cvt_pk_bf16_f32 v6, v2, v3
	v_cvt_pk_bf16_f32 v7, v4, v5
	global_store_dwordx2 v[8:9], v[6:7], off sc1
	s_waitcnt vmcnt(31)
	v_mul_f32_e32 v10, 0x3fb8aa3b, v121
	v_exp_f32_e32 v10, v10
	v_lshlrev_b32_e32 v8, 16, v92
	v_and_b32_e32 v9, 0xffff0000, v92
	v_lshlrev_b32_e32 v32, 16, v93
	v_and_b32_e32 v33, 0xffff0000, v93
	v_pk_fma_f32 v[2:3], v[2:3], v[10:11], v[8:9] op_sel_hi:[1,0,1]
	v_pk_fma_f32 v[4:5], v[4:5], v[10:11], v[32:33] op_sel_hi:[1,0,1]
	s_mov_b64 s[14:15], 0x9d44000
	v_lshl_add_u64 v[8:9], v[24:25], 0, s[14:15]
	v_cvt_pk_bf16_f32 v6, v2, v3
	v_cvt_pk_bf16_f32 v7, v4, v5
	global_store_dwordx2 v[8:9], v[6:7], off sc1
	s_waitcnt vmcnt(31)
	v_mul_f32_e32 v10, 0x3fb8aa3b, v122
	v_exp_f32_e32 v10, v10
	v_lshlrev_b32_e32 v8, 16, v94
	v_and_b32_e32 v9, 0xffff0000, v94
	v_lshlrev_b32_e32 v32, 16, v95
	v_and_b32_e32 v33, 0xffff0000, v95
	v_pk_fma_f32 v[2:3], v[2:3], v[10:11], v[8:9] op_sel_hi:[1,0,1]
	v_pk_fma_f32 v[4:5], v[4:5], v[10:11], v[32:33] op_sel_hi:[1,0,1]
	s_mov_b64 s[14:15], 0x9d55000
	v_lshl_add_u64 v[8:9], v[24:25], 0, s[14:15]
	v_cvt_pk_bf16_f32 v6, v2, v3
	v_cvt_pk_bf16_f32 v7, v4, v5
	global_store_dwordx2 v[8:9], v[6:7], off sc1
	s_waitcnt vmcnt(31)
	v_mul_f32_e32 v10, 0x3fb8aa3b, v123
	v_exp_f32_e32 v10, v10
	v_lshlrev_b32_e32 v8, 16, v96
	v_and_b32_e32 v9, 0xffff0000, v96
	v_lshlrev_b32_e32 v32, 16, v97
	v_and_b32_e32 v33, 0xffff0000, v97
	v_pk_fma_f32 v[2:3], v[2:3], v[10:11], v[8:9] op_sel_hi:[1,0,1]
	v_pk_fma_f32 v[4:5], v[4:5], v[10:11], v[32:33] op_sel_hi:[1,0,1]
	s_mov_b64 s[14:15], 0x9d66000
	v_lshl_add_u64 v[8:9], v[24:25], 0, s[14:15]
	v_cvt_pk_bf16_f32 v6, v2, v3
	v_cvt_pk_bf16_f32 v7, v4, v5
	global_store_dwordx2 v[8:9], v[6:7], off sc1
	s_waitcnt vmcnt(31)
	v_mul_f32_e32 v10, 0x3fb8aa3b, v124
	v_exp_f32_e32 v10, v10
	v_lshlrev_b32_e32 v8, 16, v98
	v_and_b32_e32 v9, 0xffff0000, v98
	v_lshlrev_b32_e32 v32, 16, v99
	v_and_b32_e32 v33, 0xffff0000, v99
	v_pk_fma_f32 v[2:3], v[2:3], v[10:11], v[8:9] op_sel_hi:[1,0,1]
	v_pk_fma_f32 v[4:5], v[4:5], v[10:11], v[32:33] op_sel_hi:[1,0,1]
	s_mov_b64 s[14:15], 0x9d77000
	v_lshl_add_u64 v[8:9], v[24:25], 0, s[14:15]
	v_cvt_pk_bf16_f32 v6, v2, v3
	v_cvt_pk_bf16_f32 v7, v4, v5
	global_store_dwordx2 v[8:9], v[6:7], off sc1
	s_waitcnt vmcnt(31)
	v_mul_f32_e32 v10, 0x3fb8aa3b, v125
	v_exp_f32_e32 v10, v10
	v_lshlrev_b32_e32 v8, 16, v100
	v_and_b32_e32 v9, 0xffff0000, v100
	v_lshlrev_b32_e32 v32, 16, v101
	v_and_b32_e32 v33, 0xffff0000, v101
	v_pk_fma_f32 v[2:3], v[2:3], v[10:11], v[8:9] op_sel_hi:[1,0,1]
	v_pk_fma_f32 v[4:5], v[4:5], v[10:11], v[32:33] op_sel_hi:[1,0,1]
	s_mov_b64 s[14:15], 0x9d88000
	v_lshl_add_u64 v[8:9], v[24:25], 0, s[14:15]
	v_cvt_pk_bf16_f32 v6, v2, v3
	v_cvt_pk_bf16_f32 v7, v4, v5
	global_store_dwordx2 v[8:9], v[6:7], off sc1
	s_waitcnt vmcnt(31)
	v_mul_f32_e32 v10, 0x3fb8aa3b, v126
	v_exp_f32_e32 v10, v10
	v_lshlrev_b32_e32 v8, 16, v102
	v_and_b32_e32 v9, 0xffff0000, v102
	v_lshlrev_b32_e32 v32, 16, v103
	v_and_b32_e32 v33, 0xffff0000, v103
	v_pk_fma_f32 v[2:3], v[2:3], v[10:11], v[8:9] op_sel_hi:[1,0,1]
	v_pk_fma_f32 v[4:5], v[4:5], v[10:11], v[32:33] op_sel_hi:[1,0,1]
	s_mov_b64 s[14:15], 0x9d99000
	v_lshl_add_u64 v[8:9], v[24:25], 0, s[14:15]
	v_cvt_pk_bf16_f32 v6, v2, v3
	v_cvt_pk_bf16_f32 v7, v4, v5
	global_store_dwordx2 v[8:9], v[6:7], off sc1
	s_waitcnt vmcnt(31)
	v_mul_f32_e32 v10, 0x3fb8aa3b, v127
	v_exp_f32_e32 v10, v10
	v_lshlrev_b32_e32 v8, 16, v104
	v_and_b32_e32 v9, 0xffff0000, v104
	v_lshlrev_b32_e32 v32, 16, v105
	v_and_b32_e32 v33, 0xffff0000, v105
	v_pk_fma_f32 v[2:3], v[2:3], v[10:11], v[8:9] op_sel_hi:[1,0,1]
	v_pk_fma_f32 v[4:5], v[4:5], v[10:11], v[32:33] op_sel_hi:[1,0,1]
	s_mov_b64 s[14:15], 0x9daa000
	v_lshl_add_u64 v[8:9], v[24:25], 0, s[14:15]
	v_cvt_pk_bf16_f32 v6, v2, v3
	v_cvt_pk_bf16_f32 v7, v4, v5
	global_store_dwordx2 v[8:9], v[6:7], off sc1
	s_waitcnt vmcnt(31)
	v_mul_f32_e32 v10, 0x3fb8aa3b, v128
	v_exp_f32_e32 v10, v10
	v_lshlrev_b32_e32 v8, 16, v108
	v_and_b32_e32 v9, 0xffff0000, v108
	v_lshlrev_b32_e32 v32, 16, v109
	v_and_b32_e32 v33, 0xffff0000, v109
	v_pk_fma_f32 v[2:3], v[2:3], v[10:11], v[8:9] op_sel_hi:[1,0,1]
	v_pk_fma_f32 v[4:5], v[4:5], v[10:11], v[32:33] op_sel_hi:[1,0,1]
	s_mov_b64 s[14:15], 0x9dbb000
	v_lshl_add_u64 v[8:9], v[24:25], 0, s[14:15]
	v_cvt_pk_bf16_f32 v6, v2, v3
	v_cvt_pk_bf16_f32 v7, v4, v5
	global_store_dwordx2 v[8:9], v[6:7], off sc1
	s_waitcnt vmcnt(31)
	v_mul_f32_e32 v10, 0x3fb8aa3b, v129
	v_exp_f32_e32 v10, v10
	v_lshlrev_b32_e32 v8, 16, v110
	v_and_b32_e32 v9, 0xffff0000, v110
	v_lshlrev_b32_e32 v32, 16, v111
	v_and_b32_e32 v33, 0xffff0000, v111
	v_pk_fma_f32 v[2:3], v[2:3], v[10:11], v[8:9] op_sel_hi:[1,0,1]
	v_pk_fma_f32 v[4:5], v[4:5], v[10:11], v[32:33] op_sel_hi:[1,0,1]
	s_mov_b64 s[14:15], 0x9dcc000
	v_lshl_add_u64 v[8:9], v[24:25], 0, s[14:15]
	v_cvt_pk_bf16_f32 v6, v2, v3
	v_cvt_pk_bf16_f32 v7, v4, v5
	global_store_dwordx2 v[8:9], v[6:7], off sc1
	s_waitcnt vmcnt(31)
	v_mul_f32_e32 v10, 0x3fb8aa3b, v26
	v_exp_f32_e32 v10, v10
	v_lshlrev_b32_e32 v8, 16, v112
	v_and_b32_e32 v9, 0xffff0000, v112
	v_lshlrev_b32_e32 v32, 16, v113
	v_and_b32_e32 v33, 0xffff0000, v113
	v_pk_fma_f32 v[2:3], v[2:3], v[10:11], v[8:9] op_sel_hi:[1,0,1]
	v_pk_fma_f32 v[4:5], v[4:5], v[10:11], v[32:33] op_sel_hi:[1,0,1]
	s_mov_b64 s[14:15], 0x9ddd000
	v_lshl_add_u64 v[8:9], v[24:25], 0, s[14:15]
	v_cvt_pk_bf16_f32 v6, v2, v3
	v_cvt_pk_bf16_f32 v7, v4, v5
	global_store_dwordx2 v[8:9], v[6:7], off sc1
	s_waitcnt vmcnt(31)
	v_mul_f32_e32 v10, 0x3fb8aa3b, v27
	v_exp_f32_e32 v10, v10
	v_lshlrev_b32_e32 v8, 16, v114
	v_and_b32_e32 v9, 0xffff0000, v114
	v_lshlrev_b32_e32 v32, 16, v115
	v_and_b32_e32 v33, 0xffff0000, v115
	v_pk_fma_f32 v[2:3], v[2:3], v[10:11], v[8:9] op_sel_hi:[1,0,1]
	v_pk_fma_f32 v[4:5], v[4:5], v[10:11], v[32:33] op_sel_hi:[1,0,1]
	s_mov_b64 s[14:15], 0x9dee000
	v_lshl_add_u64 v[8:9], v[24:25], 0, s[14:15]
	v_cvt_pk_bf16_f32 v6, v2, v3
	v_cvt_pk_bf16_f32 v7, v4, v5
	global_store_dwordx2 v[8:9], v[6:7], off sc1
	s_waitcnt vmcnt(31)
	v_mul_f32_e32 v10, 0x3fb8aa3b, v28
	v_exp_f32_e32 v10, v10
	v_lshlrev_b32_e32 v8, 16, v116
	v_and_b32_e32 v9, 0xffff0000, v116
	v_lshlrev_b32_e32 v32, 16, v117
	v_and_b32_e32 v33, 0xffff0000, v117
	v_pk_fma_f32 v[2:3], v[2:3], v[10:11], v[8:9] op_sel_hi:[1,0,1]
	v_pk_fma_f32 v[4:5], v[4:5], v[10:11], v[32:33] op_sel_hi:[1,0,1]
	s_mov_b64 s[14:15], 0x9dff000
	v_lshl_add_u64 v[8:9], v[24:25], 0, s[14:15]
	v_cvt_pk_bf16_f32 v6, v2, v3
	v_cvt_pk_bf16_f32 v7, v4, v5
	global_store_dwordx2 v[8:9], v[6:7], off sc1
	v_add_u32_e32 v1, s9, v1
	s_mov_b32 s13, 0x10fff
	v_cmp_lt_i32_e32 vcc, s13, v1
	s_or_b64 s[6:7], vcc, s[6:7]
	s_andn2_b64 exec, exec, s[6:7]
	s_cbranch_execnz .LBB0_484
